# union4 + attention LDS-DMA issue: redundant m0 save/restore dropped from the 12 asm blocks (every LDS-DMA sets m0 itself)
# baseline (speedup 1.0000x reference)
; #define GAS __attribute__((address_space(1)))
; #define LAS __attribute__((address_space(3)))
; #define WG_BAR() do { asm volatile("s_waitcnt vmcnt(0) lgkmcnt(0)" ::: "memory"); __builtin_amdgcn_s_barrier(); asm volatile("" ::: "memory"); } while (0)
; __device__ __forceinline__ int swap23(int i) { return (i & 0x13) | ((i & 4) << 1) | ((i & 8) >> 1); }
; __device__ __forceinline__ unsigned tr_off(int lane, int c, int t) { const int h = lane >> 5, blk = (lane >> 4) & 1, q = (lane & 15) >> 2, p = lane & 3; return offb(8 * h + 4 * t + q, 4 * c + 2 * blk + (p >> 1)) + 8u * (unsigned)(p & 1); }
; __device__ __forceinline__ void attn_unit(LAS unsigned char* lds, const bf16* proj, bf16* Y, const float* relb, const float* hgain, float lam, float oscale, int b, int h, int qb, int tid, int lane, int wid, Stopwatch& sw) {
;     ...
;     const int r32 = lane & 31, hi = lane >> 5, mp = wid >> 2, wq = wid & 3;
;     const int q0 = qb * 128, qw = q0 + 32 * wq;
;     const size_t rowbase = (size_t)b * SEQ;
;     LAS float* tab = (LAS float*)(lds + 98304);
;     if (tid < 129) tab[tid] = relb[t5_bucket(tid) * 8 + h] * LOG2E;
;     const float bias31 = relb[31 * 8 + h] * LOG2E;
;     LAS unsigned char* qlds = lds + 100352 + wid * 4096 + hi * 512 + r32 * 16;
;     { const bf16* qp = proj + (rowbase + qw + r32) * LDP + C_QD + h * 128 + mp * 64 + hi * 8;
; #pragma unroll
;       for (int d0 = 0; d0 < 4; ++d0) *(LAS bf16x8*)(qlds + d0 * 1024) = *(const GAS bf16x8*)(qp + d0 * 16); }
;     const bf16* k0src = proj + (rowbase + (lane & 32) + swap23(r32)) * LDP + C_KD + h * 128 + wid * 8;
;     const bf16* k1src = k0src + 64;
;     const bf16* vsrc[2];
; #pragma unroll
;     for (int i = 0; i < 2; ++i) { const int vrow = 8 * wid + 4 * i + (lane >> 4); const int ch = (lane & 15) ^ (((vrow & 3) << 2) | ((vrow >> 2) & 3)); vsrc[i] = proj + (rowbase + vrow) * LDP + C_VD + h * 128 + ch * 8; }
;     ...
;     unsigned va[4][2];
; #pragma unroll
;     for (int c = 0; c < 4; ++c) { va[c][0] = 16384u + tr_off(lane, c, 0); va[c][1] = 16384u + tr_off(lane, c, 1); }
;     const unsigned kboff = mp * 8192 + hi * 1024 + r32 * 16;
;     const int NT = 2 * qb + 2;
;     ATT_DMA(0, lds); ATT_DMA(1, lds + 32768);
;     float m_run = -1e30f, l_run = 0.f;
;     f32x16 o[4];
; #pragma unroll
;     for (int c = 0; c < 4; ++c) o[c] = splat16(0.f);
;     const int qi = qw + r32;
;     ...
;     WG_BAR();
.LBB0_360:
	s_or_b64 exec, exec, s[36:37]
	s_ashr_i32 s24, s3, 6
	s_lshl_b32 s5, s19, 7
	v_readlane_b32 s3, v252, 60
	v_and_b32_e32 v60, 31, v61
	s_or_b32 s16, s5, s3
	s_ashr_i32 s25, s24, 31
	s_lshl_b64 s[36:37], s[24:25], 12
	v_or_b32_e32 v64, s16, v60
	v_or_b32_e32 v151, s36, v64
	v_mov_b64_e32 v[20:21], s[12:13]
	v_mad_u64_u32 v[4:5], s[24:25], v151, s33, v[20:21]
	s_lshl_b32 s3, s0, 2
	v_readlane_b32 s40, v250, 2
	v_mad_i32_i24 v5, s37, v239, v5
	s_lshl_b32 s34, s0, 8
	v_bfe_u32 v44, v61, 5, 1
	v_mov_b32_e32 v2, s3
	v_readlane_b32 s42, v250, 4
	v_readlane_b32 s43, v250, 5
	v_lshl_add_u64 v[4:5], v[4:5], 0, s[34:35]
	s_lshl_b32 s24, s31, 1
	s_mov_b32 s25, s35
	v_lshl_add_u64 v[4:5], v[4:5], 0, s[24:25]
	s_movk_i32 s3, 0x3000
	global_load_dword v34, v2, s[42:43] offset:992
	v_lshlrev_b32_e32 v2, 4, v44
	v_lshl_add_u64 v[4:5], v[4:5], 0, v[2:3]
	s_mov_b64 s[24:25], 0x3800
	v_add_co_u32_e32 v16, vcc, s3, v4
	v_lshl_add_u64 v[12:13], v[4:5], 0, s[24:25]
	s_nop 0
	v_addc_co_u32_e32 v17, vcc, 0, v5, vcc
	global_load_dwordx4 v[4:7], v[12:13], off offset:32
	global_load_dwordx4 v[8:11], v[12:13], off offset:64
	s_nop 0
	global_load_dwordx4 v[12:15], v[12:13], off offset:96
	s_nop 0
	global_load_dwordx4 v[16:19], v[16:17], off offset:2048
	v_bfe_u32 v26, v61, 4, 2
	v_readlane_b32 s3, v252, 58
	v_lshlrev_b32_e32 v22, 1, v61
	v_lshrrev_b32_e32 v63, 1, v61
	v_and_b32_e32 v24, 51, v61
	v_readlane_b32 s18, v252, 61
	v_and_b32_e32 v28, 15, v61
	v_lshl_add_u32 v30, v44, 9, s3
	v_lshlrev_b32_e32 v31, 4, v60
	v_lshlrev_b32_e32 v35, 2, v26
	v_readlane_b32 s3, v252, 59
	v_and_b32_e32 v32, 8, v22
	v_and_or_b32 v24, v63, 4, v24
	v_or_b32_e32 v22, s18, v26
	v_lshlrev_b32_e32 v33, 10, v44
	v_add_u32_e32 v62, v30, v31
	v_bitop3_b32 v30, v35, v28, s3 bitop3:0x36
	v_readlane_b32 s3, v252, 62
	v_mov_b32_e32 v23, v3
	v_mov_b32_e32 v27, v3
	v_or_b32_e32 v26, 4, v22
	v_lshrrev_b32_e32 v164, 1, v60
	v_xor_b32_e32 v164, v164, v44
	v_and_b32_e32 v164, 1, v164
	v_lshlrev_b32_e32 v164, 4, v164
	v_bfe_u32 v206, v60, 2, 2
	v_lshl_or_b32 v164, v206, 5, v164
	v_lshl_or_b32 v164, v60, 7, v164
	v_or_b32_e32 v164, s3, v164
	v_or3_b32 v31, v24, v32, s36
	v_lshl_add_u64 v[22:23], s[36:37], 0, v[22:23]
	v_lshlrev_b32_e32 v24, 4, v30
	v_bfe_u32 v36, v26, 2, 2
	v_lshl_add_u64 v[26:27], s[36:37], 0, v[26:27]
	v_mad_u64_u32 v[30:31], s[24:25], v31, s33, v[20:21]
	v_mad_u64_u32 v[32:33], s[24:25], v22, s33, v[20:21]
	v_bitop3_b32 v22, v36, v28, v35 bitop3:0x36
	v_mad_u64_u32 v[20:21], s[24:25], v26, s33, v[20:21]
	v_mad_i32_i24 v31, s37, v239, v31
	s_lshl_b32 s38, s18, 1
	s_mov_b32 s39, s35
	v_mad_i32_i24 v33, v23, s33, v33
	v_mad_i32_i24 v21, v27, s33, v21
	v_lshlrev_b32_e32 v28, 4, v22
	v_lshl_add_u64 v[22:23], v[30:31], 0, s[34:35]
	v_mov_b32_e32 v25, v3
	v_mov_b32_e32 v29, v3
	v_lshl_add_u64 v[26:27], v[32:33], 0, s[34:35]
	v_lshl_add_u64 v[20:21], v[20:21], 0, s[34:35]
	v_lshl_add_u64 v[22:23], v[22:23], 0, s[38:39]
	v_and_b32_e32 v206, 63, v61
	v_lshrrev_b32_e32 v207, 3, v206
	v_add_u32_e32 v207, s18, v207
	v_and_b32_e32 v208, 0x33, v207
	v_lshlrev_b32_e32 v209, 1, v207
	v_and_b32_e32 v209, 8, v209
	v_or_b32_e32 v208, v208, v209
	v_lshrrev_b32_e32 v209, 1, v207
	v_and_b32_e32 v209, 4, v209
	v_or_b32_e32 v208, v208, v209
	v_add_u32_e32 v208, s36, v208
	v_lshrrev_b32_e32 v209, 1, v207
	v_and_b32_e32 v209, 7, v209
	v_and_b32_e32 v206, 7, v206
	v_xor_b32_e32 v206, v206, v209
	v_lshlrev_b32_e32 v206, 4, v206
	v_add_u32_e32 v206, s34, v206
	v_mov_b32_e32 v207, 0
	v_lshl_add_u64 v[206:207], s[12:13], 0, v[206:207]
	v_mad_u64_u32 v[22:23], s[100:101], v208, s33, v[206:207]
	s_mov_b64 s[24:25], 0x4000
	v_lshl_add_u64 v[24:25], v[26:27], 0, v[24:25]
	v_lshl_add_u64 v[20:21], v[20:21], 0, v[28:29]
	v_lshl_add_u64 v[52:53], v[22:23], 0, s[24:25]
	s_mov_b64 s[24:25], 0x4800
	v_lshl_add_u64 v[54:55], v[24:25], 0, s[24:25]
	v_lshl_add_u64 v[58:59], v[20:21], 0, s[24:25]
	s_mov_b64 s[24:25], 0x4080
	v_readlane_b32 s18, v253, 3
	v_lshl_add_u64 v[56:57], v[22:23], 0, s[24:25]
	s_waitcnt vmcnt(3)
	ds_write_b128 v62, v[4:7] offset:1024
	s_waitcnt vmcnt(2)
	ds_write_b128 v62, v[8:11] offset:2048
	s_waitcnt vmcnt(1)
	ds_write_b128 v62, v[12:15] offset:3072
	s_waitcnt vmcnt(0)
	ds_write_b128 v62, v[16:19]
	s_mov_b32 m0, s18
	s_nop 0
	global_load_lds_dwordx4 v[52:53], off
	v_readlane_b32 s18, v252, 63
	s_mov_b32 m0, s18
	s_nop 0
	global_load_lds_dwordx4 v[56:57], off
	v_readlane_b32 s18, v253, 0
	s_mov_b32 m0, s18
	s_nop 0
	global_load_lds_dwordx4 v[54:55], off
	s_mov_b64 s[24:25], 0x1c4000
	v_readlane_b32 s18, v253, 1
	s_mov_b32 m0, s18
	s_nop 0
	global_load_lds_dwordx4 v[58:59], off
	v_lshl_add_u64 v[26:27], v[22:23], 0, s[24:25]
	s_mov_b64 s[24:25], 0x1c4080
	v_readlane_b32 s18, v253, 2
	s_mov_b32 m0, s18
	s_nop 0
	global_load_lds_dwordx4 v[26:27], off
	v_lshl_add_u64 v[22:23], v[22:23], 0, s[24:25]
	s_mov_b64 s[24:25], 0x1c4800
	v_readlane_b32 s18, v253, 4
	s_mov_b32 m0, s18
	s_nop 0
	global_load_lds_dwordx4 v[22:23], off
	v_lshl_add_u64 v[24:25], v[24:25], 0, s[24:25]
	v_readlane_b32 s18, v253, 5
	s_mov_b32 m0, s18
	s_nop 0
	global_load_lds_dwordx4 v[24:25], off
	v_lshl_add_u64 v[20:21], v[20:21], 0, s[24:25]
	v_readlane_b32 s18, v253, 6
	s_mov_b32 m0, s18
	s_nop 0
	global_load_lds_dwordx4 v[20:21], off
	v_mul_f32_e32 v204, 0x3fb8aa3b, v34
	v_cmp_gt_u32_e32 vcc, 0x60, v61
	v_add_u32_e32 v205, 0x81, v61
	s_nop 0
	v_cndmask_b32_e32 v204, v204, v246, vcc
	v_cndmask_b32_e32 v205, v205, v61, vcc
	v_lshlrev_b32_e32 v205, 2, v205
	v_add_u32_e32 v205, 0x20800, v205
	v_cmp_gt_u32_e32 vcc, 0xbf, v61
	s_and_saveexec_b64 s[100:101], vcc
	ds_write_b32 v205, v204
	s_or_b64 exec, exec, s[100:101]
	s_waitcnt vmcnt(0) lgkmcnt(0)
	s_barrier
; #define TS_END(sw, id) do { if ((id) == TSSEL && (sw).on) (sw).acc += __builtin_amdgcn_s_memrealtime() - (sw).t0; } while (0)
; #define TS_END(sw, id) do { } while (0)
; #define WG_BAR() do { asm volatile("s_waitcnt vmcnt(0) lgkmcnt(0)" ::: "memory"); __builtin_amdgcn_s_barrier(); asm volatile("" ::: "memory"); } while (0)
; #define ATT_QK(S0, S1, sbp, cin) do { S0 = splat16(cin); S1 = S0; \
;         _Pragma("unroll") for (int d0 = 0; d0 < 4; ++d0) { const bf16x8 kf0_ = *(const LAS bf16x8*)((sbp) + kboff + d0 * 2048), kf1_ = *(const LAS bf16x8*)((sbp) + kboff + d0 * 2048 + 512), q_ = *(const LAS bf16x8*)(qlds + d0 * 1024); \
;             S0 = MFMA32(kf0_, q_, S0); S1 = MFMA32(kf1_, q_, S1); } } while (0)
; __device__ __forceinline__ void attn_unit(LAS unsigned char* lds, const bf16* proj, bf16* Y, const float* relb, const float* hgain, float lam, float oscale, int b, int h, int qb, int tid, int lane, int wid, Stopwatch& sw) {
;     ...
;     WG_BAR();
;     TS_END(sw, 8);
;     f32x16 sA0, sA1, sB0, sB1;
;     typedef __bf16 bf2_t_ __attribute__((ext_vector_type(2)));
;     const bf2_t_ one2 = __builtin_bit_cast(bf2_t_, 0x3F803F80u);
;     { const bool far0 = (63 + 128 <= qw); ATT_QK(sA0, sA1, lds, far0 ? bias31 : 0.f);
;       if (!far0) {
; #pragma unroll
;           for (int r = 0; r < 16; ++r) { const int key = 16 * (r >> 3) + 8 * hi + (r & 7); const int d0_ = qi - key, d1_ = d0_ - 32;
;               const float b0 = tab[d0_ < 0 ? 0 : (d0_ > 128 ? 128 : d0_)], b1 = tab[d1_ < 0 ? 0 : (d1_ > 128 ? 128 : d1_)];
;               sA0[r] = d0_ < 0 ? -1e30f : sA0[r] + b0; sA1[r] = d1_ < 0 ? -1e30f : sA1[r] + b1; } }
	v_add_u32_e32 v45, 0, v164
	v_xor_b32_e32 v206, 32, v45
	v_xor_b32_e32 v207, 64, v45
	v_xor_b32_e32 v208, 0x60, v45
	ds_read_b128 v[36:39], v45
	ds_read_b128 v[40:43], v62
	s_cmpk_gt_u32 s16, 0xbe
	v_mul_f32_e32 v165, 0x3fb8aa3b, v34
	s_cselect_b64 vcc, -1, 0
	v_cndmask_b32_e32 v4, 0, v165, vcc
	v_mov_b32_e32 v5, v4
	v_mov_b32_e32 v6, v4
	v_mov_b32_e32 v7, v4
	v_mov_b32_e32 v8, v4
	v_mov_b32_e32 v9, v4
	v_mov_b32_e32 v10, v4
	v_mov_b32_e32 v11, v4
	v_mov_b32_e32 v12, v4
	v_mov_b32_e32 v13, v4
	v_mov_b32_e32 v14, v4
	v_mov_b32_e32 v15, v4
	v_mov_b32_e32 v16, v4
	v_mov_b32_e32 v17, v4
	v_mov_b32_e32 v18, v4
	v_mov_b32_e32 v19, v4
	v_mov_b32_e32 v163, s37
	v_lshlrev_b32_e32 v150, 3, v44
	s_waitcnt lgkmcnt(0)
	v_mfma_f32_32x32x16_bf16 v[20:35], v[36:39], v[40:43], v[4:19]
	ds_read_b128 v[36:39], v45 offset:4096
	s_and_b64 vcc, exec, vcc
	v_readlane_b32 s41, v250, 3
	v_readlane_b32 s44, v250, 6
	v_readlane_b32 s45, v250, 7
	v_readlane_b32 s46, v250, 8
	v_readlane_b32 s47, v250, 9
	s_waitcnt lgkmcnt(0)
	v_mfma_f32_32x32x16_bf16 v[4:19], v[36:39], v[40:43], v[4:19]
	ds_read_b128 v[36:39], v206
	ds_read_b128 v[40:43], v62 offset:1024
	v_readlane_b32 s48, v250, 10
	v_readlane_b32 s49, v250, 11
	v_readlane_b32 s50, v250, 12
	v_readlane_b32 s51, v250, 13
	v_readlane_b32 s52, v250, 14
	v_readlane_b32 s53, v250, 15
	s_waitcnt lgkmcnt(0)
	v_mfma_f32_32x32x16_bf16 v[20:35], v[36:39], v[40:43], v[20:35]
	ds_read_b128 v[36:39], v206 offset:4096
	v_readlane_b32 s54, v250, 16
	v_readlane_b32 s55, v250, 17
	s_waitcnt lgkmcnt(0)
	v_mfma_f32_32x32x16_bf16 v[4:19], v[36:39], v[40:43], v[4:19]
	ds_read_b128 v[36:39], v207
	ds_read_b128 v[40:43], v62 offset:2048
	s_waitcnt lgkmcnt(0)
	v_mfma_f32_32x32x16_bf16 v[20:35], v[36:39], v[40:43], v[20:35]
	ds_read_b128 v[36:39], v207 offset:4096
	s_waitcnt lgkmcnt(0)
	v_mfma_f32_32x32x16_bf16 v[4:19], v[36:39], v[40:43], v[4:19]
	ds_read_b128 v[36:39], v208
	ds_read_b128 v[40:43], v62 offset:3072
	s_waitcnt lgkmcnt(0)
	v_mfma_f32_32x32x16_bf16 v[20:35], v[36:39], v[40:43], v[20:35]
	ds_read_b128 v[36:39], v208 offset:4096
	s_waitcnt lgkmcnt(0)
	v_mfma_f32_32x32x16_bf16 v[4:19], v[36:39], v[40:43], v[4:19]
	s_cbranch_vccnz .LBB0_394
	v_sub_u32_e32 v38, v64, v150
	v_min_i32_e32 v36, 0xa0, v38
	v_subrev_u32_e32 v36, 32, v36
	v_cmp_gt_i32_e32 vcc, 32, v38
	v_cmp_lt_i32_e64 s[36:37], -1, v38
	v_mov_b32_e32 v37, 0xf149f2ca
	v_cndmask_b32_e64 v36, v36, 0, vcc
	v_lshl_add_u32 v36, v36, 2, 0
	v_add_u32_e32 v36, 0x18000, v36
	ds_read_b32 v65, v36
	v_mov_b32_e32 v36, 0xf149f2ca
	s_and_saveexec_b64 s[38:39], s[36:37]
	s_cbranch_execz .LBB0_363
	v_min_u32_e32 v36, 0x80, v38
	v_lshl_add_u32 v36, v36, 2, 0
	v_add_u32_e32 v36, 0x18000, v36
	ds_read_b32 v36, v36
	s_waitcnt lgkmcnt(0)
	v_add_f32_e32 v36, v20, v36

.LBB0_396:
	s_add_i32 s0, s25, 0
	s_add_i32 s3, s0, s96
	s_mov_b32 m0, s3
	s_nop 0
	global_load_lds_dwordx4 v[160:161], off
	s_addk_i32 s3, 0x2000
	s_mov_b32 m0, s3
	s_nop 0
	global_load_lds_dwordx4 v[158:159], off
	s_add_i32 s0, s0, s97
	s_add_i32 s3, s0, 0x4000
	s_mov_b32 m0, s3
	s_nop 0
	global_load_lds_dwordx4 v[156:157], off
	s_addk_i32 s0, 0x4400
	s_mov_b32 m0, s0
	s_nop 0
	global_load_lds_dwordx4 v[154:155], off
